# prep LoRA weight staging: all 48 global loads issued up front then cvt+ds_write (was 6 serialized load/wait rounds)
# baseline (speedup 1.0000x reference)
.LBB0_962:
	s_bfe_u32 s50, s2, 0x30003
	s_lshl_b32 s40, s50, 6
	s_mov_b32 s51, 0
	s_mov_b32 s66, 0x8e00
	s_barrier
	s_load_dwordx2 s[12:13], s[18:19], 0x58
	s_load_dwordx2 s[14:15], s[18:19], 0x68
	s_load_dwordx2 s[16:17], s[18:19], 0x78
	s_lshl_b32 s66, s40, 2
	s_lshl_b32 s51, s34, 17
	s_waitcnt lgkmcnt(0)
	s_add_u32 s16, s16, s26
	s_addc_u32 s17, s17, s27
	s_add_u32 s0, s12, s51
	s_addc_u32 s1, s13, 0
	s_add_u32 s0, s0, s66
	s_addc_u32 s1, s1, 0
	v_lshl_add_u64 v[2:3], s[0:1], 0, v[194:195]
	v_lshl_add_u64 v[4:5], v[2:3], 0, v[162:163]
	global_load_dword v16, v[4:5], off
	v_lshl_add_u64 v[6:7], v[2:3], 0, v[164:165]
	global_load_dword v17, v[6:7], off
	v_lshl_add_u64 v[8:9], v[2:3], 0, v[166:167]
	global_load_dword v18, v[8:9], off
	v_lshl_add_u64 v[10:11], v[2:3], 0, v[168:169]
	global_load_dword v19, v[10:11], off
	v_lshl_add_u64 v[4:5], v[2:3], 0, v[170:171]
	global_load_dword v20, v[4:5], off
	v_lshl_add_u64 v[6:7], v[2:3], 0, v[172:173]
	global_load_dword v21, v[6:7], off
	v_lshl_add_u64 v[8:9], v[2:3], 0, v[174:175]
	global_load_dword v22, v[8:9], off
	v_lshl_add_u64 v[10:11], v[2:3], 0, v[176:177]
	global_load_dword v23, v[10:11], off
	s_add_u32 s0, s0, 0x20000
	s_addc_u32 s1, s1, 0
	v_lshl_add_u64 v[2:3], s[0:1], 0, v[194:195]
	v_lshl_add_u64 v[4:5], v[2:3], 0, v[162:163]
	global_load_dword v24, v[4:5], off
	v_lshl_add_u64 v[6:7], v[2:3], 0, v[164:165]
	global_load_dword v25, v[6:7], off
	v_lshl_add_u64 v[8:9], v[2:3], 0, v[166:167]
	global_load_dword v26, v[8:9], off
	v_lshl_add_u64 v[10:11], v[2:3], 0, v[168:169]
	global_load_dword v27, v[10:11], off
	v_lshl_add_u64 v[4:5], v[2:3], 0, v[170:171]
	global_load_dword v28, v[4:5], off
	v_lshl_add_u64 v[6:7], v[2:3], 0, v[172:173]
	global_load_dword v29, v[6:7], off
	v_lshl_add_u64 v[8:9], v[2:3], 0, v[174:175]
	global_load_dword v30, v[8:9], off
	v_lshl_add_u64 v[10:11], v[2:3], 0, v[176:177]
	global_load_dword v31, v[10:11], off
	s_add_u32 s0, s14, s51
	s_addc_u32 s1, s15, 0
	s_add_u32 s0, s0, s66
	s_addc_u32 s1, s1, 0
	v_lshl_add_u64 v[2:3], s[0:1], 0, v[194:195]
	v_lshl_add_u64 v[4:5], v[2:3], 0, v[162:163]
	global_load_dword v32, v[4:5], off
	v_lshl_add_u64 v[6:7], v[2:3], 0, v[164:165]
	global_load_dword v33, v[6:7], off
	v_lshl_add_u64 v[8:9], v[2:3], 0, v[166:167]
	global_load_dword v34, v[8:9], off
	v_lshl_add_u64 v[10:11], v[2:3], 0, v[168:169]
	global_load_dword v35, v[10:11], off
	v_lshl_add_u64 v[4:5], v[2:3], 0, v[170:171]
	global_load_dword v36, v[4:5], off
	v_lshl_add_u64 v[6:7], v[2:3], 0, v[172:173]
	global_load_dword v37, v[6:7], off
	v_lshl_add_u64 v[8:9], v[2:3], 0, v[174:175]
	global_load_dword v38, v[8:9], off
	v_lshl_add_u64 v[10:11], v[2:3], 0, v[176:177]
	global_load_dword v39, v[10:11], off
	s_add_u32 s0, s0, 0x20000
	s_addc_u32 s1, s1, 0
	v_lshl_add_u64 v[2:3], s[0:1], 0, v[194:195]
	v_lshl_add_u64 v[4:5], v[2:3], 0, v[162:163]
	global_load_dword v40, v[4:5], off
	v_lshl_add_u64 v[6:7], v[2:3], 0, v[164:165]
	global_load_dword v41, v[6:7], off
	v_lshl_add_u64 v[8:9], v[2:3], 0, v[166:167]
	global_load_dword v42, v[8:9], off
	v_lshl_add_u64 v[10:11], v[2:3], 0, v[168:169]
	global_load_dword v43, v[10:11], off
	v_lshl_add_u64 v[4:5], v[2:3], 0, v[170:171]
	global_load_dword v44, v[4:5], off
	v_lshl_add_u64 v[6:7], v[2:3], 0, v[172:173]
	global_load_dword v45, v[6:7], off
	v_lshl_add_u64 v[8:9], v[2:3], 0, v[174:175]
	global_load_dword v46, v[8:9], off
	v_lshl_add_u64 v[10:11], v[2:3], 0, v[176:177]
	global_load_dword v47, v[10:11], off
	s_add_u32 s0, s16, s66
	s_addc_u32 s1, s17, 0
	v_lshl_add_u64 v[2:3], s[0:1], 0, v[194:195]
	v_lshl_add_u64 v[4:5], v[2:3], 0, v[162:163]
	global_load_dword v48, v[4:5], off
	v_lshl_add_u64 v[6:7], v[2:3], 0, v[164:165]
	global_load_dword v49, v[6:7], off
	v_lshl_add_u64 v[8:9], v[2:3], 0, v[166:167]
	global_load_dword v50, v[8:9], off
	v_lshl_add_u64 v[10:11], v[2:3], 0, v[168:169]
	global_load_dword v51, v[10:11], off
	v_lshl_add_u64 v[4:5], v[2:3], 0, v[170:171]
	global_load_dword v52, v[4:5], off
	v_lshl_add_u64 v[6:7], v[2:3], 0, v[172:173]
	global_load_dword v53, v[6:7], off
	v_lshl_add_u64 v[8:9], v[2:3], 0, v[174:175]
	global_load_dword v54, v[8:9], off
	v_lshl_add_u64 v[10:11], v[2:3], 0, v[176:177]
	global_load_dword v55, v[10:11], off
	s_add_u32 s0, s0, 0x20000
	s_addc_u32 s1, s1, 0
	v_lshl_add_u64 v[2:3], s[0:1], 0, v[194:195]
	v_lshl_add_u64 v[4:5], v[2:3], 0, v[162:163]
	global_load_dword v56, v[4:5], off
	v_lshl_add_u64 v[6:7], v[2:3], 0, v[164:165]
	global_load_dword v57, v[6:7], off
	v_lshl_add_u64 v[8:9], v[2:3], 0, v[166:167]
	global_load_dword v58, v[8:9], off
	v_lshl_add_u64 v[10:11], v[2:3], 0, v[168:169]
	global_load_dword v59, v[10:11], off
	v_lshl_add_u64 v[4:5], v[2:3], 0, v[170:171]
	global_load_dword v60, v[4:5], off
	v_lshl_add_u64 v[6:7], v[2:3], 0, v[172:173]
	global_load_dword v61, v[6:7], off
	v_lshl_add_u64 v[8:9], v[2:3], 0, v[174:175]
	global_load_dword v62, v[8:9], off
	v_lshl_add_u64 v[10:11], v[2:3], 0, v[176:177]
	global_load_dword v63, v[10:11], off
	v_mul_u32_u24_e32 v3, 0x90, v155
	s_movk_i32 s0, 0x110
	v_add_u32_e32 v3, v3, v159
	v_mul_u32_u24_e32 v4, s0, v155
	v_add_u32_e32 v4, v4, v159
	s_waitcnt vmcnt(47)
	v_cvt_pk_bf16_f32 v5, v16, s0
	ds_write_b16 v3, v5 offset:0
	s_waitcnt vmcnt(46)
	v_cvt_pk_bf16_f32 v6, v17, s0
	ds_write_b16 v3, v6 offset:16
	s_waitcnt vmcnt(45)
	v_cvt_pk_bf16_f32 v7, v18, s0
	ds_write_b16 v3, v7 offset:32
	s_waitcnt vmcnt(44)
	v_cvt_pk_bf16_f32 v8, v19, s0
	ds_write_b16 v3, v8 offset:48
	s_waitcnt vmcnt(43)
	v_cvt_pk_bf16_f32 v5, v20, s0
	ds_write_b16 v3, v5 offset:64
	s_waitcnt vmcnt(42)
	v_cvt_pk_bf16_f32 v6, v21, s0
	ds_write_b16 v3, v6 offset:80
	s_waitcnt vmcnt(41)
	v_cvt_pk_bf16_f32 v7, v22, s0
	ds_write_b16 v3, v7 offset:96
	s_waitcnt vmcnt(40)
	v_cvt_pk_bf16_f32 v8, v23, s0
	ds_write_b16 v3, v8 offset:112
	s_waitcnt vmcnt(39)
	v_cvt_pk_bf16_f32 v5, v24, s0
	ds_write_b16 v3, v5 offset:9216
	s_waitcnt vmcnt(38)
	v_cvt_pk_bf16_f32 v6, v25, s0
	ds_write_b16 v3, v6 offset:9232
	s_waitcnt vmcnt(37)
	v_cvt_pk_bf16_f32 v7, v26, s0
	ds_write_b16 v3, v7 offset:9248
	s_waitcnt vmcnt(36)
	v_cvt_pk_bf16_f32 v8, v27, s0
	ds_write_b16 v3, v8 offset:9264
	s_waitcnt vmcnt(35)
	v_cvt_pk_bf16_f32 v5, v28, s0
	ds_write_b16 v3, v5 offset:9280
	s_waitcnt vmcnt(34)
	v_cvt_pk_bf16_f32 v6, v29, s0
	ds_write_b16 v3, v6 offset:9296
	s_waitcnt vmcnt(33)
	v_cvt_pk_bf16_f32 v7, v30, s0
	ds_write_b16 v3, v7 offset:9312
	s_waitcnt vmcnt(32)
	v_cvt_pk_bf16_f32 v8, v31, s0
	ds_write_b16 v3, v8 offset:9328
	s_waitcnt vmcnt(31)
	v_cvt_pk_bf16_f32 v5, v32, s0
	ds_write_b16 v3, v5 offset:18432
	s_waitcnt vmcnt(30)
	v_cvt_pk_bf16_f32 v6, v33, s0
	ds_write_b16 v3, v6 offset:18448
	s_waitcnt vmcnt(29)
	v_cvt_pk_bf16_f32 v7, v34, s0
	ds_write_b16 v3, v7 offset:18464
	s_waitcnt vmcnt(28)
	v_cvt_pk_bf16_f32 v8, v35, s0
	ds_write_b16 v3, v8 offset:18480
	s_waitcnt vmcnt(27)
	v_cvt_pk_bf16_f32 v5, v36, s0
	ds_write_b16 v3, v5 offset:18496
	s_waitcnt vmcnt(26)
	v_cvt_pk_bf16_f32 v6, v37, s0
	ds_write_b16 v3, v6 offset:18512
	s_waitcnt vmcnt(25)
	v_cvt_pk_bf16_f32 v7, v38, s0
	ds_write_b16 v3, v7 offset:18528
	s_waitcnt vmcnt(24)
	v_cvt_pk_bf16_f32 v8, v39, s0
	ds_write_b16 v3, v8 offset:18544
	s_waitcnt vmcnt(23)
	v_cvt_pk_bf16_f32 v5, v40, s0
	ds_write_b16 v3, v5 offset:27648
	s_waitcnt vmcnt(22)
	v_cvt_pk_bf16_f32 v6, v41, s0
	ds_write_b16 v3, v6 offset:27664
	s_waitcnt vmcnt(21)
	v_cvt_pk_bf16_f32 v7, v42, s0
	ds_write_b16 v3, v7 offset:27680
	s_waitcnt vmcnt(20)
	v_cvt_pk_bf16_f32 v8, v43, s0
	ds_write_b16 v3, v8 offset:27696
	s_waitcnt vmcnt(19)
	v_cvt_pk_bf16_f32 v5, v44, s0
	ds_write_b16 v3, v5 offset:27712
	s_waitcnt vmcnt(18)
	v_cvt_pk_bf16_f32 v6, v45, s0
	ds_write_b16 v3, v6 offset:27728
	s_waitcnt vmcnt(17)
	v_cvt_pk_bf16_f32 v7, v46, s0
	ds_write_b16 v3, v7 offset:27744
	s_waitcnt vmcnt(16)
	v_cvt_pk_bf16_f32 v8, v47, s0
	ds_write_b16 v3, v8 offset:27760
	s_waitcnt vmcnt(15)
	v_cvt_pk_bf16_f32 v5, v48, s0
	ds_write_b16 v4, v5 offset:36864
	s_waitcnt vmcnt(14)
	v_cvt_pk_bf16_f32 v6, v49, s0
	ds_write_b16 v4, v6 offset:36880
	s_waitcnt vmcnt(13)
	v_cvt_pk_bf16_f32 v7, v50, s0
	ds_write_b16 v4, v7 offset:36896
	s_waitcnt vmcnt(12)
	v_cvt_pk_bf16_f32 v8, v51, s0
	ds_write_b16 v4, v8 offset:36912
	s_waitcnt vmcnt(11)
	v_cvt_pk_bf16_f32 v5, v52, s0
	ds_write_b16 v4, v5 offset:36928
	s_waitcnt vmcnt(10)
	v_cvt_pk_bf16_f32 v6, v53, s0
	ds_write_b16 v4, v6 offset:36944
	s_waitcnt vmcnt(9)
	v_cvt_pk_bf16_f32 v7, v54, s0
	ds_write_b16 v4, v7 offset:36960
	s_waitcnt vmcnt(8)
	v_cvt_pk_bf16_f32 v8, v55, s0
	ds_write_b16 v4, v8 offset:36976
	s_waitcnt vmcnt(7)
	v_cvt_pk_bf16_f32 v5, v56, s0
	ds_write_b16 v4, v5 offset:36992
	s_waitcnt vmcnt(6)
	v_cvt_pk_bf16_f32 v6, v57, s0
	ds_write_b16 v4, v6 offset:37008
	s_waitcnt vmcnt(5)
	v_cvt_pk_bf16_f32 v7, v58, s0
	ds_write_b16 v4, v7 offset:37024
	s_waitcnt vmcnt(4)
	v_cvt_pk_bf16_f32 v8, v59, s0
	ds_write_b16 v4, v8 offset:37040
	s_waitcnt vmcnt(3)
	v_cvt_pk_bf16_f32 v5, v60, s0
	ds_write_b16 v4, v5 offset:37056
	s_waitcnt vmcnt(2)
	v_cvt_pk_bf16_f32 v6, v61, s0
	ds_write_b16 v4, v6 offset:37072
	s_waitcnt vmcnt(1)
	v_cvt_pk_bf16_f32 v7, v62, s0
	ds_write_b16 v4, v7 offset:37088
	s_waitcnt vmcnt(0)
	v_cvt_pk_bf16_f32 v8, v63, s0
	ds_write_b16 v4, v8 offset:37104
